# top-k phase: waves 1-7 of the 32 top-k workgroups touch the phase's code range as data (one dword per 64-byte line) while thread 0 waits in the preceding grid barrier, so the instruction fetches hit t
# speedup vs baseline: 1.0089x; 1.0049x over previous
.LBB0_659:
	s_waitcnt vmcnt(0)
	s_barrier
	v_readfirstlane_b32 s99, v186
	v_readlane_b32 s100, v235, 16
	s_lshr_b32 s99, s99, 6
	s_cmp_eq_u32 s99, 0
	s_cbranch_scc1 .Ltkw_skip
	s_cmp_lt_u32 s100, 32
	s_cbranch_scc0 .Ltkw_skip
	s_getpc_b64 s[100:101]
.Ltkw_pc:
	s_add_u32 s100, s100, .Ltkw_code-.Ltkw_pc
	s_addc_u32 s101, s101, 0
	s_sub_u32 s99, s99, 1
	s_lshl_b32 s99, s99, 12
	v_and_b32_e32 v236, 63, v186
	v_lshlrev_b32_e32 v236, 6, v236
	v_add_u32_e32 v236, s99, v236
	global_load_dword v238, v236, s[100:101]
.Ltkw_skip:
	s_mov_b64 s[0:1], exec
	v_readlane_b32 s2, v235, 5
	v_readlane_b32 s3, v235, 6
	s_and_b64 s[2:3], s[0:1], s[2:3]
	s_xor_b64 s[0:1], s[2:3], s[0:1]
	s_mov_b64 exec, s[2:3]
	s_cbranch_execz .LBB0_712
	s_cmp_eq_u32 s98, 0
	s_cbranch_scc1 .Lxb_nopend_7
	v_readlane_b32 s100, v235, 7
	v_readlane_b32 s101, v235, 8
	v_mov_b32_e32 v237, 0x3400
	v_mov_b32_e32 v239, 0
	s_nop 3

.Ltkw_code:
.LBB0_724:
	s_andn2_b64 vcc, exec, s[0:1]
	s_cbranch_vccnz .LBB0_919
	v_mov_b32_e32 v0, v186
	s_andn2_b64 vcc, exec, s[4:5]
	s_cbranch_vccnz .LBB0_919
	s_load_dwordx2 s[0:1], s[6:7], 0x98
	v_and_b32_e32 v2, 63, v0
	v_ashrrev_i32_e32 v1, 6, v0
	v_lshlrev_b32_e32 v20, 4, v0
	v_cmp_gt_u32_e64 s[6:7], 64, v0
	s_waitcnt lgkmcnt(0)
	s_add_u32 s30, s0, 0x11b000
	s_addc_u32 s31, s1, 0
	s_add_u32 s34, s0, 0x13b000
	s_addc_u32 s35, s1, 0
	s_add_u32 s2, s0, 0x15b000
	v_writelane_b32 v235, s2, 20
	s_addc_u32 s2, s1, 0
	v_writelane_b32 v235, s2, 21
	s_movk_i32 s2, 0x100
	v_cmp_gt_i32_e64 s[4:5], s2, v0
	v_cmp_eq_u32_e64 s[2:3], 0, v2
	v_lshlrev_b32_e32 v22, 2, v0
	v_mul_lo_u32 v3, v0, 12
	v_writelane_b32 v235, s2, 22
	v_mbcnt_hi_u32_b32 v0, -1, v187
	v_and_b32_e32 v5, 63, v0
	v_writelane_b32 v235, s3, 23
	v_cmp_gt_u32_e64 s[2:3], 2, v2
	v_cmp_ne_u32_e32 vcc, 63, v5
	v_and_b32_e32 v4, 64, v0
	v_writelane_b32 v235, s2, 24
	v_addc_co_u32_e32 v6, vcc, 0, v0, vcc
	s_nop 0
	v_writelane_b32 v235, s3, 25
	v_cmp_gt_u32_e64 s[2:3], 4, v2
	v_cmp_gt_u32_e32 vcc, 62, v5
	v_lshlrev_b32_e32 v36, 2, v6
	v_writelane_b32 v235, s2, 26
	v_cndmask_b32_e64 v6, 0, 2, vcc
	v_cmp_gt_u32_e32 vcc, 60, v5
	v_writelane_b32 v235, s3, 27
	v_cmp_gt_u32_e64 s[2:3], 8, v2
	v_add_lshl_u32 v37, v6, v0, 2
	v_cndmask_b32_e64 v6, 0, 4, vcc
	v_writelane_b32 v235, s2, 28
	v_cmp_gt_u32_e32 vcc, 56, v5
	v_add_lshl_u32 v38, v6, v0, 2
	v_writelane_b32 v235, s3, 29
	v_cmp_gt_u32_e64 s[2:3], 16, v2
	v_cndmask_b32_e64 v6, 0, 8, vcc
	v_cmp_gt_u32_e32 vcc, 48, v5
	v_writelane_b32 v235, s2, 30
	s_add_u32 s36, s0, 0x25b000
	v_cndmask_b32_e64 v5, 0, 16, vcc
	v_writelane_b32 v235, s3, 31
	v_cmp_lt_i32_e64 s[2:3], 0, v1
	v_add_lshl_u32 v40, v5, v0, 2
	v_mov_b32_e32 v5, 0x80
	v_writelane_b32 v235, s2, 32
	v_lshl_or_b32 v41, v0, 2, v5
	v_add_u32_e32 v5, -1, v0
	v_writelane_b32 v235, s3, 33
	v_cmp_lt_i32_e64 s[2:3], 1, v1
	v_cmp_lt_i32_e32 vcc, v5, v4
	s_addc_u32 s37, s1, 0
	v_writelane_b32 v235, s2, 34
	v_cndmask_b32_e32 v5, v5, v0, vcc
	v_lshlrev_b32_e32 v42, 2, v5
	v_writelane_b32 v235, s3, 35
	v_cmp_lt_i32_e64 s[2:3], 2, v1
	v_add_u32_e32 v5, -2, v0
	v_cmp_lt_i32_e32 vcc, v5, v4
	v_writelane_b32 v235, s2, 36
	v_cmp_eq_u32_e64 s[8:9], 63, v2
	v_cndmask_b32_e32 v5, v5, v0, vcc
	v_writelane_b32 v235, s3, 37
	v_cmp_lt_i32_e64 s[2:3], 3, v1
	v_lshlrev_b32_e32 v43, 2, v5
	v_add_u32_e32 v5, -4, v0
	v_writelane_b32 v235, s2, 38
	v_cmp_lt_i32_e32 vcc, v5, v4
	v_cmp_gt_u32_e64 s[10:11], 62, v2
	v_writelane_b32 v235, s3, 39
	v_cmp_lt_i32_e64 s[2:3], 4, v1
	v_cndmask_b32_e32 v5, v5, v0, vcc
	v_lshlrev_b32_e32 v44, 2, v5
	v_writelane_b32 v235, s2, 40
	v_add_u32_e32 v5, -8, v0
	v_cmp_lt_i32_e32 vcc, v5, v4
	v_writelane_b32 v235, s3, 41
	v_cmp_lt_i32_e64 s[2:3], 5, v1
	v_cndmask_b32_e32 v5, v5, v0, vcc
	v_lshlrev_b32_e32 v45, 2, v5
	v_writelane_b32 v235, s2, 42
	v_add_u32_e32 v5, -16, v0
	v_cmp_gt_u32_e64 s[12:13], 60, v2
	v_writelane_b32 v235, s3, 43
	v_cmp_lt_i32_e64 s[2:3], 6, v1
	v_cmp_gt_u32_e64 s[14:15], 56, v2
	v_cmp_gt_u32_e64 s[16:17], 48, v2
	v_writelane_b32 v235, s2, 44
	v_cmp_gt_u32_e64 s[18:19], 32, v2
	v_cmp_lt_i32_e32 vcc, v5, v4
	v_writelane_b32 v235, s3, 45
	v_cmp_lt_i32_e64 s[2:3], 7, v1
	v_subrev_u32_e32 v2, 32, v0
	v_cndmask_b32_e32 v5, v5, v0, vcc
	v_writelane_b32 v235, s2, 46
	v_cmp_lt_i32_e32 vcc, v2, v4
	v_ashrrev_i32_e32 v21, 31, v20
	v_writelane_b32 v235, s3, 47
	v_add_lshl_u32 v39, v6, v0, 2
	v_readlane_b32 s24, v235, 16
	v_readlane_b32 s20, v235, 0
	v_readlane_b32 s25, v235, 17
	v_readlane_b32 s22, v235, 2
	s_lshl_b32 s33, s24, 10
	s_lshl_b32 s47, s22, 10
	s_lshl_b64 s[2:3], s[24:25], 15
	s_add_u32 s0, s0, s2
	v_cndmask_b32_e32 v0, v2, v0, vcc
	s_addc_u32 s1, s1, s3
	v_lshl_add_u32 v35, v1, 2, 0
	v_lshlrev_b32_e32 v47, 2, v0
	v_lshl_add_u64 v[0:1], v[20:21], 2, s[0:1]
	s_mov_b64 s[0:1], 0x1b000
	v_add_u32_e32 v34, 0, v22
	v_lshl_add_u64 v[30:31], v[0:1], 0, s[0:1]
	s_ashr_i32 s1, s22, 31
	s_mov_b32 s0, s22
	v_or_b32_e32 v24, 3, v22
	v_or_b32_e32 v26, 2, v22
	v_or_b32_e32 v28, 1, v22
	v_lshlrev_b32_e32 v46, 2, v5
	v_or_b32_e32 v48, 1, v20
	v_or_b32_e32 v49, 2, v20
	v_or_b32_e32 v50, 3, v20
	v_or_b32_e32 v51, 4, v20
	v_or_b32_e32 v52, 5, v20
	v_or_b32_e32 v53, 6, v20
	v_or_b32_e32 v54, 7, v20
	v_or_b32_e32 v55, 8, v20
	v_or_b32_e32 v56, 9, v20
	v_or_b32_e32 v57, 10, v20
	v_or_b32_e32 v58, 11, v20
	v_or_b32_e32 v59, 12, v20
	v_or_b32_e32 v60, 13, v20
	v_or_b32_e32 v61, 14, v20
	v_or_b32_e32 v62, 15, v20
	s_lshl_b64 s[38:39], s[0:1], 15
	v_mov_b32_e32 v21, 0
	v_mov_b32_e32 v63, 1
	s_movk_i32 s42, 0x3ff
	v_add_u32_e32 v64, v34, v3
	s_mov_b32 s43, s24
	v_readlane_b32 s21, v235, 1
	v_readlane_b32 s23, v235, 3
	s_branch .LBB0_728
